# phase-2 late tiles 6 per gMLP workgroup (was 7), dedicated phase-1 converters 6240 tiles
# speedup vs baseline: 1.0012x; 1.0012x over previous
.LBB0_86:
	s_cmp_lt_i32 s50, 2
	s_cselect_b64 s[6:7], -1, 0
	s_and_b64 s[0:1], s[6:7], s[2:3]
	s_andn2_b64 vcc, exec, s[0:1]
	v_writelane_b32 v254, s60, 4
	s_cbranch_vccnz .LBB0_260
	s_mov_b64 s[2:3], s[80:81]
	s_load_dwordx2 s[8:9], s[2:3], 0xa8
	s_cmpk_lg_i32 s56, 0x100
	s_cselect_b32 s0, s56, 0xc8
	s_cmp_ge_i32 s78, s0
	s_mov_b64 s[4:5], -1
	s_cbranch_scc0 .LBB0_145
	s_sub_i32 s1, s78, s0
	s_cmpk_gt_i32 s1, 0x185f
	s_cbranch_scc1 .LBB0_144
	s_sub_i32 s20, s56, s0
	s_abs_i32 s4, s20
	v_cvt_f32_u32_e32 v1, s4
	s_load_dwordx2 s[10:11], s[2:3], 0x78
	s_load_dwordx2 s[12:13], s[2:3], 0x88
	s_sub_i32 s2, s20, s1
	s_add_i32 s3, s2, 0x185f
	v_rcp_iflag_f32_e32 v1, v1
	s_sub_i32 s2, 0xffffe7a1, s2
	s_xor_b32 s14, s3, s20
	s_sub_i32 s5, 0, s4
	v_mul_f32_e32 v1, 0x4f7ffffe, v1
	v_cvt_u32_f32_e32 v1, v1
	s_max_i32 s2, s3, s2
	s_ashr_i32 s3, s14, 31
	v_readfirstlane_b32 s14, v1
	s_mul_i32 s5, s5, s14
	s_mul_hi_u32 s5, s14, s5
	s_add_i32 s14, s14, s5
	s_mul_hi_u32 s5, s2, s14
	s_mul_i32 s14, s5, s4
	s_sub_i32 s2, s2, s14
	s_add_i32 s14, s5, 1
	s_sub_i32 s15, s2, s4
	s_cmp_ge_u32 s2, s4
	s_cselect_b32 s5, s14, s5
	s_cselect_b32 s2, s15, s2
	s_add_i32 s14, s5, 1
	s_cmp_ge_u32 s2, s4
	s_cselect_b32 s2, s14, s5
	s_xor_b32 s2, s2, s3
	s_sub_i32 s29, s2, s3
	s_lshl_b32 s21, s29, 2
	s_add_i32 s22, s21, -1
	s_cmp_gt_i32 s29, 0
	s_cselect_b64 s[2:3], -1, 0
	s_and_b64 s[4:5], s[2:3], exec
	s_cselect_b32 s18, 0, s22
	s_ashr_i32 s4, s18, 2
	s_mul_i32 s17, s4, s20
	s_add_i32 s17, s17, s1
	s_cmpk_gt_i32 s17, 0x1fff
	s_mov_b32 s5, 0
	s_cbranch_scc0 .LBB0_91
	s_add_i32 s4, s17, 0xffffe000
	s_lshr_b32 s4, s4, 7
	s_lshl_b64 s[4:5], s[4:5], 24
	s_waitcnt lgkmcnt(0)
	s_add_u32 s14, s12, s4
	s_addc_u32 s15, s13, s5
	s_lshl_b32 s4, s17, 4
	s_and_b32 s26, s4, 0x780
	s_lshl_b32 s4, s17, 8
	s_and_b32 s16, s4, 0x700
	s_mov_b64 s[4:5], 0x800
	s_cbranch_execz .LBB0_92
	s_branch .LBB0_93

.LBB0_160:
	s_add_i32 s89, s59, -1
	s_cmp_lt_u32 s89, 8
	s_cselect_b32 s88, 1, 0
	s_cbranch_scc0 .Lp1c_skip1
	s_and_b32 s90, s89, 1
	s_lshr_b32 s91, s57, 2
	s_cmp_eq_u32 s90, s91
	s_cselect_b32 s88, 1, 0
	s_cbranch_scc0 .Lp1c_skip1
	s_lshr_b32 s89, s89, 1
	s_mul_i32 s89, s89, 200
	s_add_u32 s89, s89, s78
	s_add_u32 s89, s89, 6240
	s_cmp_lt_u32 s89, 0x2000
	s_cselect_b32 s88, 1, 0
	s_cbranch_scc0 .Lp1c_skip1
	s_lshr_b32 s90, s89, 4
	s_lshl_b32 s90, s90, 21
	s_and_b32 s91, s89, 15
	s_lshl_b32 s92, s91, 10
	s_or_b32 s90, s90, s92
	s_lshl_b32 s92, s57, 7
	s_or_b32 s90, s90, s92
	s_add_u32 s84, s82, s90
	s_addc_u32 s85, s83, 0
	s_lshr_b32 s90, s89, 8
	s_lshl_b32 s90, s90, 23
	s_lshl_b32 s91, s91, 19
	s_or_b32 s90, s90, s91
	s_bfe_u32 s91, s89, 0x40004
	s_lshl_b32 s91, s91, 7
	s_or_b32 s90, s90, s91
	s_lshl_b32 s91, s57, 15
	s_or_b32 s90, s90, s91
	s_add_u32 s90, s90, 0x4ee00000
	s_add_u32 s86, s48, s90
	s_addc_u32 s87, s49, 0
	global_load_dwordx4 v[180:183], v245, s[84:85] nt
	s_add_u32 s84, s84, 0x4000
	s_addc_u32 s85, s85, 0
	global_load_dwordx4 v[184:187], v245, s[84:85] nt
	s_add_u32 s84, s84, 0x4000
	s_addc_u32 s85, s85, 0
	global_load_dwordx4 v[188:191], v245, s[84:85] nt
	s_add_u32 s84, s84, 0x4000
	s_addc_u32 s85, s85, 0
	global_load_dwordx4 v[192:195], v245, s[84:85] nt
	s_add_u32 s84, s84, 0x4000
	s_addc_u32 s85, s85, 0
	global_load_dwordx4 v[196:199], v245, s[84:85] nt
	s_add_u32 s84, s84, 0x4000
	s_addc_u32 s85, s85, 0
	global_load_dwordx4 v[200:203], v245, s[84:85] nt
	s_add_u32 s84, s84, 0x4000
	s_addc_u32 s85, s85, 0
	global_load_dwordx4 v[204:207], v245, s[84:85] nt
	s_add_u32 s84, s84, 0x4000
	s_addc_u32 s85, s85, 0
	global_load_dwordx4 v[208:211], v245, s[84:85] nt
	s_add_u32 s84, s84, 0x4000
	s_addc_u32 s85, s85, 0
	global_load_dwordx4 v[212:215], v245, s[84:85] nt
	s_add_u32 s84, s84, 0x4000
	s_addc_u32 s85, s85, 0
	global_load_dwordx4 v[216:219], v245, s[84:85] nt
	s_add_u32 s84, s84, 0x4000
	s_addc_u32 s85, s85, 0
	global_load_dwordx4 v[220:223], v245, s[84:85] nt
	s_add_u32 s84, s84, 0x4000
	s_addc_u32 s85, s85, 0
	global_load_dwordx4 v[224:227], v245, s[84:85] nt
	s_add_u32 s84, s84, 0x4000
	s_addc_u32 s85, s85, 0
	global_load_dwordx4 v[228:231], v245, s[84:85] nt
	s_add_u32 s84, s84, 0x4000
	s_addc_u32 s85, s85, 0
	global_load_dwordx4 v[232:235], v245, s[84:85] nt
	s_add_u32 s84, s84, 0x4000
	s_addc_u32 s85, s85, 0
	global_load_dwordx4 v[236:239], v245, s[84:85] nt
	s_add_u32 s84, s84, 0x4000
	s_addc_u32 s85, s85, 0
	global_load_dwordx4 v[240:243], v245, s[84:85] nt

.LBB0_367:
	s_lshr_b32 s0, s56, 31
	s_add_i32 s0, s56, s0
	s_ashr_i32 s0, s0, 1
	v_readlane_b32 s78, v254, 5
	s_cmp_ge_i32 s78, s0
	v_readlane_b32 s79, v254, 8
	v_readlane_b32 s60, v254, 4
	s_cbranch_scc0 .LBB0_409
	s_sub_i32 s10, s78, s0
	s_cmpk_gt_u32 s10, 0x37f
	s_waitcnt vmcnt(0) lgkmcnt(0)
	s_barrier
	s_cbranch_scc1 .LBB0_409
	s_sub_i32 s0, s56, s0
	s_abs_i32 s2, s0
	v_cvt_f32_u32_e32 v2, s2
	s_sub_i32 s3, s0, s10
	s_add_i32 s4, s3, 0x37f
	s_sub_i32 s3, 0xfffffc81, s3
	v_rcp_iflag_f32_e32 v2, v2
	s_xor_b32 s6, s4, s0
	s_sub_i32 s5, 0, s2
	s_max_i32 s3, s4, s3
	v_mul_f32_e32 v2, 0x4f7ffffe, v2
	v_cvt_u32_f32_e32 v2, v2
	s_ashr_i32 s4, s6, 31
	s_add_i32 s1, s10, 0x2000
	v_readfirstlane_b32 s6, v2
	s_mul_i32 s5, s5, s6
	s_mul_hi_u32 s5, s6, s5
	s_add_i32 s6, s6, s5
	s_mul_hi_u32 s5, s3, s6
	s_mul_i32 s6, s5, s2
	s_sub_i32 s3, s3, s6
	s_add_i32 s7, s5, 1
	s_sub_i32 s6, s3, s2
	s_cmp_ge_u32 s3, s2
	s_cselect_b32 s5, s7, s5
	s_cselect_b32 s3, s6, s3
	s_add_i32 s6, s5, 1
	s_cmp_ge_u32 s3, s2
	s_cselect_b32 s2, s6, s5
	s_xor_b32 s2, s2, s4
	s_sub_i32 s18, s2, s4
	s_mov_b32 s18, 6
	s_movk_i32 s0, 0xff80
	s_lshl_b32 s12, s18, 2
	s_add_i32 s13, s12, -1
	s_cmp_gt_i32 s18, 0
	s_cselect_b64 s[2:3], -1, 0
	s_and_b64 s[4:5], s[2:3], exec
	s_cselect_b32 s11, 0, s13
	s_ashr_i32 s4, s11, 2
	s_mul_i32 s9, s4, s0
	s_add_i32 s9, s9, s1
	s_cmpk_gt_i32 s9, 0x1fff
	s_mov_b32 s5, 0
	s_cbranch_scc0 .LBB0_371
	s_add_i32 s4, s9, 0xffffe000
	s_lshr_b32 s4, s4, 7
	s_lshl_b64 s[4:5], s[4:5], 24
	v_readlane_b32 s34, v254, 13
	v_readlane_b32 s35, v254, 14
	s_add_u32 s6, s34, s4
	s_addc_u32 s7, s35, s5
	s_lshl_b32 s4, s9, 4
	s_and_b32 s19, s4, 0x780
	s_lshl_b32 s4, s9, 8
	v_readlane_b32 s30, v254, 11
	s_and_b32 s8, s4, 0x700
	v_readlane_b32 s31, v254, 12
	s_mov_b64 s[4:5], 0x800
	s_cbranch_execz .LBB0_372
	s_branch .LBB0_373

.LBB0_537:
	s_add_i32 s89, s58, -1
	s_cmp_lt_u32 s89, 2
	s_cselect_b32 s88, 1, 0
	s_cbranch_scc0 .Lp4c_skip1
	s_mul_i32 s89, s89, 256
	s_add_u32 s89, s89, s78
	s_add_u32 s89, s89, 7040
	s_cmp_lt_u32 s89, 0x2000
	s_cselect_b32 s88, 1, 0
	s_cbranch_scc0 .Lp4c_skip1
	s_lshr_b32 s90, s89, 4
	s_lshl_b32 s90, s90, 21
	s_and_b32 s91, s89, 15
	s_lshl_b32 s92, s91, 10
	s_or_b32 s90, s90, s92
	s_lshl_b32 s92, s57, 7
	s_or_b32 s90, s90, s92
	s_add_u32 s84, s82, s90
	s_addc_u32 s85, s83, 0
	s_lshr_b32 s90, s89, 8
	s_lshl_b32 s90, s90, 23
	s_lshl_b32 s91, s91, 19
	s_or_b32 s90, s90, s91
	s_bfe_u32 s91, s89, 0x40004
	s_lshl_b32 s91, s91, 7
	s_or_b32 s90, s90, s91
	s_lshl_b32 s91, s57, 15
	s_or_b32 s90, s90, s91
	s_add_u32 s90, s90, 0x4ee00000
	s_add_u32 s86, s48, s90
	s_addc_u32 s87, s49, 0
	global_load_dwordx4 v[180:183], v245, s[84:85] nt
	s_add_u32 s84, s84, 0x4000
	s_addc_u32 s85, s85, 0
	global_load_dwordx4 v[184:187], v245, s[84:85] nt
	s_add_u32 s84, s84, 0x4000
	s_addc_u32 s85, s85, 0
	global_load_dwordx4 v[188:191], v245, s[84:85] nt
	s_add_u32 s84, s84, 0x4000
	s_addc_u32 s85, s85, 0
	global_load_dwordx4 v[192:195], v245, s[84:85] nt
	s_add_u32 s84, s84, 0x4000
	s_addc_u32 s85, s85, 0
	global_load_dwordx4 v[196:199], v245, s[84:85] nt
	s_add_u32 s84, s84, 0x4000
	s_addc_u32 s85, s85, 0
	global_load_dwordx4 v[200:203], v245, s[84:85] nt
	s_add_u32 s84, s84, 0x4000
	s_addc_u32 s85, s85, 0
	global_load_dwordx4 v[204:207], v245, s[84:85] nt
	s_add_u32 s84, s84, 0x4000
	s_addc_u32 s85, s85, 0
	global_load_dwordx4 v[208:211], v245, s[84:85] nt
	s_add_u32 s84, s84, 0x4000
	s_addc_u32 s85, s85, 0
	global_load_dwordx4 v[212:215], v245, s[84:85] nt
	s_add_u32 s84, s84, 0x4000
	s_addc_u32 s85, s85, 0
	global_load_dwordx4 v[216:219], v245, s[84:85] nt
	s_add_u32 s84, s84, 0x4000
	s_addc_u32 s85, s85, 0
	global_load_dwordx4 v[220:223], v245, s[84:85] nt
	s_add_u32 s84, s84, 0x4000
	s_addc_u32 s85, s85, 0
	global_load_dwordx4 v[224:227], v245, s[84:85] nt
	s_add_u32 s84, s84, 0x4000
	s_addc_u32 s85, s85, 0
	global_load_dwordx4 v[228:231], v245, s[84:85] nt
	s_add_u32 s84, s84, 0x4000
	s_addc_u32 s85, s85, 0
	global_load_dwordx4 v[232:235], v245, s[84:85] nt
	s_add_u32 s84, s84, 0x4000
	s_addc_u32 s85, s85, 0
	global_load_dwordx4 v[236:239], v245, s[84:85] nt
	s_add_u32 s84, s84, 0x4000
	s_addc_u32 s85, s85, 0
	global_load_dwordx4 v[240:243], v245, s[84:85] nt
